# speedup vs baseline: 1.0425x; 1.0134x over previous
_Z11attn_kernelPKDF16_S0_S0_PDF16_PKfS1_:
	s_lshl_b32 s12, s2, 2
	s_and_b32 s3, s12, 12
	s_ashr_i32 s4, s2, 6
	s_add_i32 s3, s3, s4
	s_add_i32 s4, s3, 1
	v_cvt_f32_i32_e32 v1, s4
	s_mov_b32 s4, 0xc2fc0000
	s_bfe_u32 s6, s2, 0x10002
	s_bfe_u32 s70, s2, 0x30003
	v_mul_f32_e32 v2, -0.5, v1
	v_cmp_gt_f32_e32 vcc, s4, v2
	s_and_b64 s[4:5], vcc, exec
	s_cselect_b32 s4, 0xffffffc0, 0
	s_load_dwordx8 s[60:67], s[0:1], 0x0
	s_load_dwordx4 s[8:11], s[0:1], 0x20
	s_lshl_b32 s0, s6, 4
	s_add_i32 s0, s0, s3
	s_ashr_i32 s1, s0, 31
	s_lshl_b64 s[0:1], s[0:1], 19
	s_waitcnt lgkmcnt(0)
	s_add_u32 s68, s60, s0
	s_addc_u32 s71, s61, s1
	s_lshl_b32 s0, s2, 19
	s_and_b32 s0, s0, 0x380000
	v_writelane_b32 v248, s8, 0
	s_add_u32 s74, s62, s0
	s_addc_u32 s75, s63, 0
	v_writelane_b32 v248, s9, 1
	v_writelane_b32 v248, s10, 2
	s_add_u32 s76, s64, s0
	v_writelane_b32 v248, s11, 3
	s_addc_u32 s77, s65, 0
	s_lshl_b32 s100, s70, 15
	s_add_u32 s74, s74, s100
	s_addc_u32 s75, s75, 0
	s_add_u32 s76, s76, s100
	s_addc_u32 s77, s77, 0
	s_lshl_b32 s1, s6, 11
	s_xor_b32 s0, s70, 15
	v_writelane_b32 v248, s1, 4
	s_lshl_b32 s1, s3, 7
	v_mov_b32_e32 v3, 0x42800000
	s_add_u32 s2, s74, 0x8000
	v_cndmask_b32_e32 v2, 0, v3, vcc
	v_writelane_b32 v248, s1, 5
	s_addc_u32 s3, s75, 0
	v_fmac_f32_e32 v2, -0.5, v1
	v_writelane_b32 v248, s2, 6
	v_exp_f32_e32 v1, v2
	s_mov_b32 s7, 0x3db504f3
	v_writelane_b32 v248, s3, 7
	s_add_u32 s2, s74, 0xa000
	s_addc_u32 s3, s75, 0
	v_writelane_b32 v248, s2, 8
	v_ldexp_f32 v1, v1, s4
	v_div_scale_f32 v2, s[4:5], s7, s7, v1
	v_writelane_b32 v248, s3, 9
	s_add_u32 s2, s74, 0xc000
	s_addc_u32 s3, s75, 0
	v_writelane_b32 v248, s2, 10
	v_rcp_f32_e32 v3, v2
	s_mov_b32 s73, 0
	v_writelane_b32 v248, s3, 11
	s_add_u32 s2, s74, 0xe000
	s_addc_u32 s3, s75, 0
	v_writelane_b32 v248, s2, 12
	v_fma_f32 v4, -v2, v3, 1.0
	s_or_b32 s1, s12, 2
	v_writelane_b32 v248, s3, 13
	v_writelane_b32 v248, s0, 14
	s_lshl_b32 s0, s0, 14
	v_fmac_f32_e32 v3, v4, v3
	v_div_scale_f32 v4, vcc, v1, s7, v1
	v_writelane_b32 v248, s12, 15
	s_cmp_lg_u32 s70, 0
	v_mul_f32_e32 v5, v4, v3
	v_writelane_b32 v248, s1, 16
	s_cselect_b64 s[2:3], -1, 0
	v_fma_f32 v6, -v2, v5, v4
	v_writelane_b32 v248, s2, 17
	v_fmac_f32_e32 v5, v6, v3
	s_lshl_b32 s1, s70, 15
	v_writelane_b32 v248, s3, 18
	v_fma_f32 v2, -v2, v5, v4
	v_writelane_b32 v248, s1, 19
	s_lshl_b32 s0, s0, 1
	v_div_fmas_f32 v2, v2, v3, v5
	v_writelane_b32 v248, s0, 20
	v_div_fixup_f32 v1, v2, s7, v1
	v_mov_b32_e32 v2, 0
	v_writelane_b32 v248, s70, 21
	s_mov_b64 s[62:63], -1
	v_mov_b32_e32 v158, 0x21000
	v_mov_b32_e32 v159, 0x8000
	v_mov_b32_e32 v151, 0
	s_mov_b32 s94, 0x3e0293ee
	s_mov_b64 s[96:97], 0x10000
	s_mov_b64 s[98:99], 0x12000
	s_mov_b64 s[86:87], 0x14000
	s_mov_b64 s[78:79], 0x16000
	v_mov_b32_e32 v160, 4
	v_mov_b32_e32 v161, 3
	v_mov_b32_e32 v162, 1
	v_mov_b32_e32 v163, 0x80
	v_mov_b32_e32 v164, 0xff800000
	v_mov_b32_e32 v114, 0
	v_mov_b32_e32 v115, v2
	v_mov_b32_e32 v116, v2
	v_mov_b32_e32 v117, v2
	v_mov_b32_e32 v118, 0
	v_mov_b32_e32 v119, v2
	v_mov_b32_e32 v120, v2
	v_mov_b32_e32 v121, v2
	v_mov_b32_e32 v122, 0
	v_mov_b32_e32 v123, v2
	v_mov_b32_e32 v124, v2
	v_mov_b32_e32 v125, v2
	v_mov_b32_e32 v126, 0
	v_mov_b32_e32 v127, v2
	v_mov_b32_e32 v128, v2
	v_mov_b32_e32 v129, v2
	v_mov_b32_e32 v130, 0
	v_mov_b32_e32 v131, v2
	v_mov_b32_e32 v132, v2
	v_mov_b32_e32 v133, v2
	v_mov_b32_e32 v134, 0
	v_mov_b32_e32 v135, v2
	v_mov_b32_e32 v136, v2
	v_mov_b32_e32 v137, v2
	v_mov_b32_e32 v138, 0
	v_mov_b32_e32 v139, v2
	v_mov_b32_e32 v140, v2
	v_mov_b32_e32 v141, v2
	v_mov_b32_e32 v142, 0
	v_mov_b32_e32 v143, v2
	v_mov_b32_e32 v144, v2
	v_mov_b32_e32 v145, v2
	v_writelane_b32 v248, s74, 22
	s_nop 1
	v_writelane_b32 v248, s75, 23
	s_branch .LBB1_2

.LBB1_4:
	s_and_b64 s[0:1], s[62:63], exec
	v_readlane_b32 s0, v248, 14
	s_cselect_b32 s83, s0, s70
	s_lshl_b32 s90, s83, 7
	s_lshl_b32 s89, s88, 5
	v_and_b32_e32 v167, 31, v55
	v_lshrrev_b32_e32 v5, 5, v165
	s_ashr_i32 s91, s95, 8
	s_mov_b32 s93, s89
	v_or_b32_e32 v6, s93, v167
	v_lshlrev_b32_e32 v168, 2, v5
	s_lshl_b32 s64, s91, 14
	v_sub_u32_e32 v171, v6, v168
	s_add_i32 s0, s64, 0
	s_add_i32 s0, s0, 0x10000
	s_barrier
	v_lshlrev_b32_e32 v53, 8, v167
	v_lshlrev_b32_e32 v61, 4, v5
	v_and_b32_e32 v86, 0xf0, v4
	v_bitop3_b32 v4, v61, v53, v86 bitop3:0xde
	v_add_u32_e32 v172, s0, v4
	v_xor_b32_e32 v249, 0x80, v172
	ds_read_b128 v[4:7], v172
	ds_read_b128 v[62:65], v249
	v_or_b32_e32 v8, 32, v61
	s_waitcnt lgkmcnt(0)
	v_mfma_f32_32x32x16_f16 v[20:35], v[4:7], v[114:117], 0
	ds_read_b128 v[4:7], v172 offset:8192
	ds_read_b128 v[66:69], v249 offset:8192
	v_bitop3_b32 v8, v8, v53, v86 bitop3:0xde
	v_add_u32_e32 v173, s0, v8
	v_xor_b32_e32 v253, 0x80, v173
	ds_read_b128 v[70:73], v173
	ds_read_b128 v[74:77], v253
	v_or_b32_e32 v78, 64, v61
	v_bitop3_b32 v78, v78, v53, v86 bitop3:0xde
	s_waitcnt lgkmcnt(0)
	v_mfma_f32_32x32x16_f16 v[20:35], v[70:73], v[118:121], v[20:35]
	ds_read_b128 v[70:73], v173 offset:8192
	v_add_u32_e32 v174, s0, v78
	v_xor_b32_e32 v254, 0x80, v174
	ds_read_b128 v[78:81], v253 offset:8192
	v_or_b32_e32 v61, 0x60, v61
	v_bitop3_b32 v53, v61, v53, v86 bitop3:0xde
	v_add_u32_e32 v175, s0, v53
	v_xor_b32_e32 v255, 0x80, v175
	s_lshl_b32 s82, s91, 6
	v_mfma_f32_32x32x16_f16 v[4:19], v[4:7], v[114:117], 0
	s_or_b32 s0, s82, 63
	s_cmp_le_i32 s0, s93
	v_subrev_u32_e32 v53, s82, v171
	s_waitcnt lgkmcnt(0)
	v_mfma_f32_32x32x16_f16 v[4:19], v[70:73], v[118:121], v[4:19]
	ds_read_b128 v[70:73], v174
	ds_read_b128 v[82:85], v254
	ds_read_b128 v[86:89], v254 offset:8192
	s_waitcnt lgkmcnt(0)
	v_mfma_f32_32x32x16_f16 v[20:35], v[70:73], v[122:125], v[20:35]
	ds_read_b128 v[70:73], v174 offset:8192
	s_waitcnt lgkmcnt(0)
	v_mfma_f32_32x32x16_f16 v[4:19], v[70:73], v[122:125], v[4:19]
	ds_read_b128 v[70:73], v175
	ds_read_b128 v[90:93], v255
	s_waitcnt lgkmcnt(0)
	v_mfma_f32_32x32x16_f16 v[20:35], v[70:73], v[126:129], v[20:35]
	ds_read_b128 v[70:73], v175 offset:8192
	ds_read_b128 v[94:97], v255 offset:8192
	s_waitcnt lgkmcnt(0)
	v_mfma_f32_32x32x16_f16 v[4:19], v[70:73], v[126:129], v[4:19]
	s_waitcnt vmcnt(0)
	v_mfma_f32_32x32x16_f16 v[20:35], v[62:65], v[130:133], v[20:35]
	v_mfma_f32_32x32x16_f16 v[4:19], v[66:69], v[130:133], v[4:19]
	s_waitcnt vmcnt(8)
	v_mfma_f32_32x32x16_f16 v[20:35], v[74:77], v[134:137], v[20:35]
	v_mfma_f32_32x32x16_f16 v[4:19], v[78:81], v[134:137], v[4:19]
	s_waitcnt vmcnt(7)
	v_mfma_f32_32x32x16_f16 v[20:35], v[82:85], v[138:141], v[20:35]
	v_mfma_f32_32x32x16_f16 v[4:19], v[86:89], v[138:141], v[4:19]
	s_waitcnt vmcnt(6)
	v_mfma_f32_32x32x16_f16 v[20:35], v[90:93], v[142:145], v[20:35]
	s_waitcnt lgkmcnt(0)
	v_mfma_f32_32x32x16_f16 v[4:19], v[94:97], v[142:145], v[4:19]
	s_cbranch_scc1 .LBB1_6
	v_cmp_gt_i32_e64 s[58:59], 26, v53
	v_cmp_gt_i32_e64 s[60:61], 27, v53
	v_cmp_gt_i32_e64 s[56:57], 25, v53
	s_and_b64 s[58:59], s[60:61], s[58:59]
	v_cmp_gt_i32_e64 s[54:55], 24, v53
	s_and_b64 s[56:57], s[58:59], s[56:57]
	v_cmp_gt_i32_e64 s[52:53], 19, v53
	s_and_b64 s[54:55], s[56:57], s[54:55]
	v_cmp_gt_i32_e64 s[50:51], 18, v53
	s_and_b64 s[52:53], s[54:55], s[52:53]
	v_cmp_gt_i32_e64 s[48:49], 17, v53
	s_and_b64 s[50:51], s[52:53], s[50:51]
	v_cmp_gt_i32_e64 s[46:47], 16, v53
	s_and_b64 s[48:49], s[50:51], s[48:49]
	v_cmp_gt_i32_e64 s[44:45], 11, v53
	s_and_b64 s[46:47], s[48:49], s[46:47]
	v_cmp_gt_i32_e64 s[42:43], 10, v53
	s_and_b64 s[44:45], s[46:47], s[44:45]
	v_cmp_gt_i32_e64 s[40:41], 9, v53
	s_and_b64 s[42:43], s[44:45], s[42:43]
	v_cmp_gt_i32_e64 s[38:39], 8, v53
	s_and_b64 s[40:41], s[42:43], s[40:41]
	v_cmp_gt_i32_e64 s[36:37], 3, v53
	s_and_b64 s[38:39], s[40:41], s[38:39]
	v_cmp_gt_i32_e64 s[34:35], 2, v53
	s_and_b64 s[36:37], s[38:39], s[36:37]
	v_cmp_gt_i32_e64 s[30:31], 1, v53
	s_and_b64 s[34:35], s[36:37], s[34:35]
	v_cmp_gt_i32_e64 s[28:29], 0, v53
	s_and_b64 s[30:31], s[34:35], s[30:31]
	s_and_b64 s[28:29], s[30:31], s[28:29]
	v_cmp_gt_i32_e64 s[26:27], 58, v53
	v_cndmask_b32_e64 v20, v20, v164, s[28:29]
	v_cmp_gt_i32_e64 s[28:29], 59, v53
	v_cmp_gt_i32_e64 s[24:25], 57, v53
	s_and_b64 s[26:27], s[28:29], s[26:27]
	v_cmp_gt_i32_e64 s[22:23], 56, v53
	s_and_b64 s[24:25], s[26:27], s[24:25]
	v_cmp_gt_i32_e64 s[20:21], 51, v53
	s_and_b64 s[22:23], s[24:25], s[22:23]
	v_cmp_gt_i32_e64 s[18:19], 50, v53
	s_and_b64 s[20:21], s[22:23], s[20:21]
	v_cmp_gt_i32_e64 s[16:17], 49, v53
	s_and_b64 s[18:19], s[20:21], s[18:19]
	v_cmp_gt_i32_e64 s[14:15], 48, v53
	s_and_b64 s[16:17], s[18:19], s[16:17]
	v_cmp_gt_i32_e64 s[12:13], 43, v53
	s_and_b64 s[14:15], s[16:17], s[14:15]
	v_cmp_gt_i32_e64 s[10:11], 42, v53
	s_and_b64 s[12:13], s[14:15], s[12:13]
	v_cmp_gt_i32_e64 s[8:9], 41, v53
	s_and_b64 s[10:11], s[12:13], s[10:11]
	v_cmp_gt_i32_e64 s[6:7], 40, v53
	s_and_b64 s[8:9], s[10:11], s[8:9]
	v_cmp_gt_i32_e64 s[4:5], 35, v53
	s_and_b64 s[6:7], s[8:9], s[6:7]
	v_cmp_gt_i32_e64 s[2:3], 34, v53
	s_and_b64 s[4:5], s[6:7], s[4:5]
	v_cmp_gt_i32_e64 s[0:1], 33, v53
	s_and_b64 s[2:3], s[4:5], s[2:3]
	v_cmp_gt_i32_e32 vcc, 32, v53
	s_and_b64 s[0:1], s[2:3], s[0:1]
	s_and_b64 vcc, s[0:1], vcc
	v_cndmask_b32_e64 v35, v35, v164, s[60:61]
	v_cndmask_b32_e64 v34, v34, v164, s[58:59]
	v_cndmask_b32_e64 v33, v33, v164, s[56:57]
	v_cndmask_b32_e64 v32, v32, v164, s[54:55]
	v_cndmask_b32_e64 v31, v31, v164, s[52:53]
	v_cndmask_b32_e64 v30, v30, v164, s[50:51]
	v_cndmask_b32_e64 v29, v29, v164, s[48:49]
	v_cndmask_b32_e64 v28, v28, v164, s[46:47]
	v_cndmask_b32_e64 v27, v27, v164, s[44:45]
	v_cndmask_b32_e64 v26, v26, v164, s[42:43]
	v_cndmask_b32_e64 v25, v25, v164, s[40:41]
	v_cndmask_b32_e64 v24, v24, v164, s[38:39]
	v_cndmask_b32_e64 v23, v23, v164, s[36:37]
	v_cndmask_b32_e64 v22, v22, v164, s[34:35]
	v_cndmask_b32_e64 v21, v21, v164, s[30:31]
	v_cndmask_b32_e64 v19, v19, v164, s[28:29]
	v_cndmask_b32_e64 v18, v18, v164, s[26:27]
	v_cndmask_b32_e64 v17, v17, v164, s[24:25]
	v_cndmask_b32_e64 v16, v16, v164, s[22:23]
	v_cndmask_b32_e64 v15, v15, v164, s[20:21]
	v_cndmask_b32_e64 v14, v14, v164, s[18:19]
	v_cndmask_b32_e64 v13, v13, v164, s[16:17]
	v_cndmask_b32_e64 v12, v12, v164, s[14:15]
	v_cndmask_b32_e64 v11, v11, v164, s[12:13]
	v_cndmask_b32_e64 v10, v10, v164, s[10:11]
	v_cndmask_b32_e64 v9, v9, v164, s[8:9]
	v_cndmask_b32_e64 v8, v8, v164, s[6:7]
	v_cndmask_b32_e64 v7, v7, v164, s[4:5]
	v_cndmask_b32_e64 v6, v6, v164, s[2:3]
	v_cndmask_b32_e64 v5, v5, v164, s[0:1]
	v_cndmask_b32_e32 v4, v4, v164, vcc

.LBB1_8:
	s_mov_b32 s2, 0xf149f2ca
	v_max3_f32 v178, v61, v62, s2
	v_fma_f32 v3, -v1, v53, -v178
	s_waitcnt vmcnt(3)
	v_mul_f32_e32 v36, 0x3e0293ee, v3
	v_fmamk_f32 v3, v20, 0x3e0293ee, v36
	s_lshl_b32 s2, s33, 9
	v_exp_f32_e32 v190, v3
	v_sub_f32_e32 v3, 0xf149f2ca, v178
	s_add_i32 s92, s2, 0
	v_fmamk_f32 v20, v21, 0x3e0293ee, v36
	v_fmamk_f32 v21, v22, 0x3e0293ee, v36
	v_fmamk_f32 v22, v23, 0x3e0293ee, v36
	v_fmamk_f32 v23, v24, 0x3e0293ee, v36
	v_fmamk_f32 v24, v25, 0x3e0293ee, v36
	v_fmamk_f32 v25, v26, 0x3e0293ee, v36
	v_fmamk_f32 v26, v27, 0x3e0293ee, v36
	v_fmamk_f32 v27, v28, 0x3e0293ee, v36
	v_fmamk_f32 v28, v29, 0x3e0293ee, v36
	v_fmamk_f32 v29, v30, 0x3e0293ee, v36
	v_fmamk_f32 v30, v31, 0x3e0293ee, v36
	v_fmamk_f32 v31, v32, 0x3e0293ee, v36
	v_fmamk_f32 v32, v33, 0x3e0293ee, v36
	v_fmamk_f32 v33, v34, 0x3e0293ee, v36
	v_fmamk_f32 v34, v35, 0x3e0293ee, v36
	v_mul_f32_e32 v3, 0x3e0293ee, v3
	v_pk_fma_f32 v[98:99], v[4:5], s[94:95], v[36:37] op_sel_hi:[1,0,0]
	s_add_i32 s92, s92, 0x20000
	v_lshlrev_b32_e32 v4, 4, v165
	v_exp_f32_e32 v191, v20
	v_exp_f32_e32 v188, v21
	v_exp_f32_e32 v189, v22
	v_exp_f32_e32 v186, v23
	v_exp_f32_e32 v187, v24
	v_exp_f32_e32 v184, v25
	v_exp_f32_e32 v185, v26
	v_exp_f32_e32 v182, v27
	v_exp_f32_e32 v183, v28
	v_exp_f32_e32 v156, v29
	v_exp_f32_e32 v157, v30
	v_exp_f32_e32 v148, v31
	v_exp_f32_e32 v149, v32
	v_exp_f32_e32 v146, v33
	v_exp_f32_e32 v147, v34
	v_exp_f32_e32 v170, v3
	s_cmp_lg_u32 0, -1
	v_lshlrev_b32_e32 v3, 3, v165
	v_and_b32_e32 v4, 0xc0, v4
	v_lshlrev_b32_e32 v5, 1, v165
	v_pk_fma_f32 v[100:101], v[6:7], s[94:95], v[36:37] op_sel_hi:[1,0,0]
	s_cselect_b32 s2, 0, 0
	v_and_or_b32 v4, v3, 24, v4
	v_and_b32_e32 v5, 32, v5
	v_and_b32_e32 v6, 0x100, v3
	s_add_i32 s64, s64, s2
	v_or3_b32 v4, v4, v5, v6
	v_pk_fma_f32 v[112:113], v[18:19], s[94:95], v[36:37] op_sel_hi:[1,0,0]
	v_pk_fma_f32 v[110:111], v[16:17], s[94:95], v[36:37] op_sel_hi:[1,0,0]
	v_pk_fma_f32 v[108:109], v[14:15], s[94:95], v[36:37] op_sel_hi:[1,0,0]
	v_pk_fma_f32 v[106:107], v[12:13], s[94:95], v[36:37] op_sel_hi:[1,0,0]
	v_pk_fma_f32 v[104:105], v[10:11], s[94:95], v[36:37] op_sel_hi:[1,0,0]
	v_pk_fma_f32 v[102:103], v[8:9], s[94:95], v[36:37] op_sel_hi:[1,0,0]
	s_mov_b32 s72, 1
	v_add_u32_e32 v169, s64, v4
	s_cmp_lt_u32 s83, 2
	s_barrier
	s_cbranch_scc1 .LBB1_25
	s_lshl_b32 s5, s95, 3
	s_and_b32 s5, s5, 0xfffffe00
	v_or_b32_e32 v4, s5, v3
	s_add_i32 s5, s89, 0x100
	s_nop 0
	v_add_u32_e32 v3, s5, v167
	v_ashrrev_i32_e32 v5, 31, v4
	v_sub_u32_e32 v3, v3, v168
	v_mov_b32_e32 v16, v2
	v_mov_b32_e32 v17, v2
	s_lshl_b32 s4, s33, 10
	v_lshlrev_b64 v[154:155], 1, v[4:5]
	v_add_u32_e32 v250, 0x2000, v154
	v_add_u32_e32 v251, 0x4000, v154
	v_add_u32_e32 v252, 0x6000, v154
	v_subrev_u32_e32 v179, s82, v3
	v_mov_b32_e32 v3, v2
	v_mov_b32_e32 v4, v2
	v_mov_b32_e32 v5, v2
	v_mov_b32_e32 v6, v2
	v_mov_b32_e32 v7, v2
	v_mov_b32_e32 v8, v2
	v_mov_b32_e32 v9, v2
	v_mov_b32_e32 v10, v2
	v_mov_b32_e32 v11, v2
	v_mov_b32_e32 v12, v2
	v_mov_b32_e32 v13, v2
	v_mov_b32_e32 v14, v2
	v_mov_b32_e32 v15, v2
	s_waitcnt vmcnt(0)
	v_mov_b64_e32 v[48:49], v[16:17]
	v_mov_b64_e32 v[80:81], v[16:17]
	v_mov_b64_e32 v[32:33], v[16:17]
	v_mov_b64_e32 v[64:65], v[16:17]
	s_mov_b32 s70, s68
	v_cmp_gt_u32_e64 s[2:3], 32, v165
	v_lshl_add_u32 v176, v167, 2, s92
	v_lshl_add_u32 v177, v168, 2, s92
	s_mov_b32 s68, 0xfff00000
	v_mov_b32_e32 v166, 0
	s_add_i32 s69, s4, 0
	s_mov_b64 s[84:85], s[76:77]
	v_mov_b64_e32 v[46:47], v[14:15]
	v_mov_b64_e32 v[44:45], v[12:13]
	v_mov_b64_e32 v[42:43], v[10:11]
	v_mov_b64_e32 v[40:41], v[8:9]
	v_mov_b64_e32 v[38:39], v[6:7]
	v_mov_b64_e32 v[36:37], v[4:5]
	v_mov_b64_e32 v[34:35], v[2:3]
	v_mov_b64_e32 v[78:79], v[14:15]
	v_mov_b64_e32 v[76:77], v[12:13]
	v_mov_b64_e32 v[74:75], v[10:11]
	v_mov_b64_e32 v[72:73], v[8:9]
	v_mov_b64_e32 v[70:71], v[6:7]
	v_mov_b64_e32 v[68:69], v[4:5]
	v_mov_b64_e32 v[66:67], v[2:3]
	v_mov_b64_e32 v[30:31], v[14:15]
	v_mov_b64_e32 v[28:29], v[12:13]
	v_mov_b64_e32 v[26:27], v[10:11]
	v_mov_b64_e32 v[24:25], v[8:9]
	v_mov_b64_e32 v[22:23], v[6:7]
	v_mov_b64_e32 v[20:21], v[4:5]
	v_mov_b64_e32 v[18:19], v[2:3]
	v_mov_b64_e32 v[62:63], v[14:15]
	v_mov_b64_e32 v[60:61], v[12:13]
	v_mov_b64_e32 v[58:59], v[10:11]
	v_mov_b64_e32 v[56:57], v[8:9]
	v_mov_b64_e32 v[54:55], v[6:7]
	v_mov_b64_e32 v[52:53], v[4:5]
	v_mov_b64_e32 v[50:51], v[2:3]
	s_branch .LBB1_12
.LBB1_10:
	s_or_b64 exec, exec, s[4:5]
	ds_read_b128 v[198:201], v177 offset:224
	ds_read_b128 v[202:205], v177 offset:192
	ds_read_b128 v[206:209], v177 offset:160
	ds_read_b128 v[210:213], v177 offset:128
	s_branch .LBB1_11
.Llazy2:
	v_mov_b32_e32 v178, v182
	v_mov_b32_e32 v5, 1.0
.LBB1_11:
	v_fma_f32 v4, -v1, v16, -v178
	v_mul_f32_e32 v4, 0x3e0293ee, v4
	v_fmamk_f32 v6, v98, 0x3e0293ee, v4
	v_fmamk_f32 v7, v99, 0x3e0293ee, v4
	v_fmamk_f32 v8, v100, 0x3e0293ee, v4
	v_fmamk_f32 v9, v101, 0x3e0293ee, v4
	v_fmamk_f32 v10, v102, 0x3e0293ee, v4
	v_fmamk_f32 v11, v103, 0x3e0293ee, v4
	v_fmamk_f32 v12, v104, 0x3e0293ee, v4
	v_fmamk_f32 v13, v105, 0x3e0293ee, v4
	v_fmamk_f32 v14, v106, 0x3e0293ee, v4
	v_fmamk_f32 v15, v107, 0x3e0293ee, v4
	v_fmamk_f32 v16, v108, 0x3e0293ee, v4
	v_fmamk_f32 v17, v109, 0x3e0293ee, v4
	v_fmamk_f32 v98, v110, 0x3e0293ee, v4
	v_fmamk_f32 v99, v111, 0x3e0293ee, v4
	v_fmamk_f32 v100, v112, 0x3e0293ee, v4
	v_fmamk_f32 v101, v113, 0x3e0293ee, v4
	s_add_u32 s76, s76, 0x10000
	v_exp_f32_e32 v190, v6
	v_exp_f32_e32 v191, v7
	v_exp_f32_e32 v188, v8
	v_exp_f32_e32 v189, v9
	v_exp_f32_e32 v186, v10
	v_exp_f32_e32 v187, v11
	v_exp_f32_e32 v184, v12
	v_exp_f32_e32 v185, v13
	v_exp_f32_e32 v182, v14
	v_exp_f32_e32 v183, v15
	v_exp_f32_e32 v156, v16
	v_exp_f32_e32 v157, v17
	v_exp_f32_e32 v148, v98
	v_exp_f32_e32 v149, v99
	v_exp_f32_e32 v146, v100
	v_exp_f32_e32 v147, v101
	s_addc_u32 s77, s77, 0
	s_addk_i32 s68, 0x100
	v_add_f32_e32 v3, v3, v180
	s_add_u32 s74, s74, 0x10000
	v_fmac_f32_e32 v3, v170, v166
	v_add_f32_e32 v166, v192, v193
	s_addc_u32 s75, s75, 0
	v_pk_fma_f32 v[112:113], v[96:97], s[94:95], v[4:5] op_sel_hi:[1,0,0]
	v_pk_fma_f32 v[110:111], v[94:95], s[94:95], v[4:5] op_sel_hi:[1,0,0]
	v_pk_fma_f32 v[108:109], v[92:93], s[94:95], v[4:5] op_sel_hi:[1,0,0]
	v_pk_fma_f32 v[106:107], v[90:91], s[94:95], v[4:5] op_sel_hi:[1,0,0]
	v_pk_fma_f32 v[104:105], v[88:89], s[94:95], v[4:5] op_sel_hi:[1,0,0]
	v_pk_fma_f32 v[102:103], v[86:87], s[94:95], v[4:5] op_sel_hi:[1,0,0]
	v_pk_fma_f32 v[100:101], v[84:85], s[94:95], v[4:5] op_sel_hi:[1,0,0]
	v_pk_fma_f32 v[98:99], v[82:83], s[94:95], v[4:5] op_sel_hi:[1,0,0]
	v_fmac_f32_e32 v166, v3, v181
	s_cmp_lt_u32 s72, s83
	v_add_u32_e32 v179, 0x100, v179
	v_mov_b32_e32 v170, v5
	s_cbranch_vccz .Lnoresc2
	s_waitcnt lgkmcnt(0)
	v_pk_mul_f32 v[64:65], v[64:65], v[200:201]
	v_pk_mul_f32 v[60:61], v[60:61], v[204:205]
	v_pk_mul_f32 v[56:57], v[56:57], v[208:209]
	v_pk_mul_f32 v[52:53], v[52:53], v[212:213]
	v_pk_mul_f32 v[62:63], v[62:63], v[198:199]
	v_pk_mul_f32 v[58:59], v[58:59], v[202:203]
	v_pk_mul_f32 v[54:55], v[54:55], v[206:207]
	v_pk_mul_f32 v[50:51], v[50:51], v[210:211]
	v_pk_mul_f32 v[32:33], v[32:33], v[200:201]
	v_pk_mul_f32 v[28:29], v[28:29], v[204:205]
	v_pk_mul_f32 v[24:25], v[24:25], v[208:209]
	v_pk_mul_f32 v[20:21], v[20:21], v[212:213]
	v_pk_mul_f32 v[30:31], v[30:31], v[198:199]
	v_pk_mul_f32 v[26:27], v[26:27], v[202:203]
	v_pk_mul_f32 v[22:23], v[22:23], v[206:207]
	v_pk_mul_f32 v[18:19], v[18:19], v[210:211]
	v_pk_mul_f32 v[80:81], v[80:81], v[200:201]
	v_pk_mul_f32 v[76:77], v[76:77], v[204:205]
	v_pk_mul_f32 v[72:73], v[72:73], v[208:209]
	v_pk_mul_f32 v[68:69], v[68:69], v[212:213]
	v_pk_mul_f32 v[78:79], v[78:79], v[198:199]
	v_pk_mul_f32 v[74:75], v[74:75], v[202:203]
	v_pk_mul_f32 v[70:71], v[70:71], v[206:207]
	v_pk_mul_f32 v[66:67], v[66:67], v[210:211]
	v_pk_mul_f32 v[48:49], v[48:49], v[200:201]
	v_pk_mul_f32 v[44:45], v[44:45], v[204:205]
	v_pk_mul_f32 v[40:41], v[40:41], v[208:209]
	v_pk_mul_f32 v[36:37], v[36:37], v[212:213]
	v_pk_mul_f32 v[46:47], v[46:47], v[198:199]
	v_pk_mul_f32 v[42:43], v[42:43], v[202:203]
	v_pk_mul_f32 v[38:39], v[38:39], v[206:207]
	v_pk_mul_f32 v[34:35], v[34:35], v[210:211]

.LBB1_12:
	ds_read_b128 v[4:7], v172 offset:32768
	ds_read_b128 v[8:11], v249 offset:32768
	ds_read_b128 v[192:195], v172 offset:40960
	ds_read_b128 v[196:199], v249 offset:40960
	ds_read_b128 v[12:15], v173 offset:32768
	ds_read_b128 v[200:203], v253 offset:32768
	ds_read_b128 v[204:207], v173 offset:40960
	ds_read_b128 v[208:211], v253 offset:40960
	s_waitcnt lgkmcnt(7)
	v_mfma_f32_32x32x16_f16 v[82:97], v[4:7], v[114:117], 0
	ds_read_b128 v[4:7], v174 offset:32768
	ds_read_b128 v[212:215], v254 offset:32768
	ds_read_b128 v[216:219], v174 offset:40960
	ds_read_b128 v[220:223], v254 offset:40960
	ds_read_b128 v[224:227], v175 offset:32768
	ds_read_b128 v[228:231], v255 offset:32768
	ds_read_b128 v[232:235], v175 offset:40960
	ds_read_b128 v[236:239], v255 offset:40960
	v_add_f32_e32 v3, 0, v190
	v_add_f32_e32 v3, v191, v3
	v_add_f32_e32 v3, v188, v3
	v_add_f32_e32 v3, v189, v3
	v_add_f32_e32 v3, v186, v3
	v_add_f32_e32 v3, v187, v3
	s_waitcnt lgkmcnt(11)
	v_mfma_f32_32x32x16_f16 v[82:97], v[12:15], v[118:121], v[82:97]
	v_add_f32_e32 v3, v184, v3
	v_add_f32_e32 v3, v185, v3
	v_add_f32_e32 v3, v182, v3
	v_add_f32_e32 v3, v183, v3
	v_add_f32_e32 v3, v156, v3
	v_add_f32_e32 v3, v157, v3
	v_exp_f32_e32 v12, v98
	s_waitcnt lgkmcnt(7)
	v_mfma_f32_32x32x16_f16 v[82:97], v[4:7], v[122:125], v[82:97]
	v_add_f32_e32 v3, v148, v3
	v_exp_f32_e32 v13, v99
	v_add_f32_e32 v3, v149, v3
	v_exp_f32_e32 v14, v100
	v_add_f32_e32 v3, v146, v3
	v_exp_f32_e32 v15, v101
	v_add_f32_e32 v3, v147, v3
	s_waitcnt lgkmcnt(3)
	v_mfma_f32_32x32x16_f16 v[82:97], v[224:227], v[126:129], v[82:97]
	v_exp_f32_e32 v16, v102
	v_add_f32_e32 v3, v12, v3
	v_exp_f32_e32 v17, v103
	v_add_f32_e32 v3, v13, v3
	v_exp_f32_e32 v98, v104
	v_add_f32_e32 v3, v14, v3
	v_exp_f32_e32 v99, v105
	v_mfma_f32_32x32x16_f16 v[82:97], v[8:11], v[130:133], v[82:97]
	v_add_f32_e32 v3, v15, v3
	v_exp_f32_e32 v100, v106
	v_add_f32_e32 v3, v16, v3
	v_exp_f32_e32 v101, v107
	v_add_f32_e32 v3, v17, v3
	v_exp_f32_e32 v102, v108
	v_add_f32_e32 v3, v98, v3
	v_mfma_f32_32x32x16_f16 v[82:97], v[200:203], v[134:137], v[82:97]
	v_exp_f32_e32 v103, v109
	v_add_f32_e32 v3, v99, v3
	v_exp_f32_e32 v104, v110
	v_add_f32_e32 v3, v100, v3
	v_exp_f32_e32 v105, v111
	v_add_f32_e32 v3, v101, v3
	v_exp_f32_e32 v106, v112
	v_mfma_f32_32x32x16_f16 v[82:97], v[212:215], v[138:141], v[82:97]
	v_add_f32_e32 v3, v102, v3
	v_exp_f32_e32 v107, v113
	v_add_f32_e32 v3, v103, v3
	v_add_f32_e32 v3, v104, v3
	v_add_f32_e32 v3, v105, v3
	v_add_f32_e32 v3, v106, v3
	v_add_f32_e32 v3, v107, v3
	s_waitcnt lgkmcnt(2)
	v_mfma_f32_32x32x16_f16 v[82:97], v[228:231], v[142:145], v[82:97]
	v_mov_b32_e32 v180, v3
	v_cvt_pk_f16_f32 v4, v190, v191
	v_cvt_pk_f16_f32 v5, v188, v189
	v_cvt_pk_f16_f32 v6, v186, v187
	v_cvt_pk_f16_f32 v7, v184, v185
	v_cvt_pk_f16_f32 v8, v182, v183
	v_cvt_pk_f16_f32 v9, v156, v157
	v_cvt_pk_f16_f32 v10, v148, v149
	v_cvt_pk_f16_f32 v11, v146, v147
	v_cvt_pk_f16_f32 v12, v12, v13
	v_cvt_pk_f16_f32 v13, v14, v15
	v_cvt_pk_f16_f32 v14, v16, v17
	v_cvt_pk_f16_f32 v15, v98, v99
	v_cvt_pk_f16_f32 v146, v100, v101
	v_cvt_pk_f16_f32 v147, v102, v103
	v_cvt_pk_f16_f32 v148, v104, v105
	v_cvt_pk_f16_f32 v149, v106, v107
	s_nop 1
	v_permlane32_swap_b32_e32 v3, v180
	v_permlane32_swap_b32_e32 v4, v6
	v_permlane32_swap_b32_e32 v5, v7
	v_permlane32_swap_b32_e32 v8, v10
	v_permlane32_swap_b32_e32 v9, v11
	v_permlane32_swap_b32_e32 v12, v14
	v_permlane32_swap_b32_e32 v13, v15
	v_permlane32_swap_b32_e32 v146, v148
	v_permlane32_swap_b32_e32 v147, v149
	s_add_u32 s4, s74, 0x10000
	s_addc_u32 s5, s75, 0
	s_add_u32 s6, s76, 0x8000
	s_addc_u32 s7, s77, 0
	s_add_i32 m0, s69, 0x10000
	v_mfma_f32_32x32x16_f16 v[98:113], v[192:195], v[114:117], 0
	global_load_lds_dwordx4 v154, s[4:5]
	s_add_i32 m0, s69, 0x12000
	v_mfma_f32_32x32x16_f16 v[98:113], v[204:207], v[118:121], v[98:113]
	global_load_lds_dwordx4 v250, s[4:5]
	s_add_i32 m0, s69, 0x14000
	v_mfma_f32_32x32x16_f16 v[98:113], v[216:219], v[122:125], v[98:113]
	global_load_lds_dwordx4 v251, s[4:5]
	s_add_i32 m0, s69, 0x16000
	s_waitcnt lgkmcnt(0)
	v_mfma_f32_32x32x16_f16 v[98:113], v[232:235], v[126:129], v[98:113]
	global_load_lds_dwordx4 v252, s[4:5]
	s_add_i32 m0, s69, 0x8000
	v_mfma_f32_32x32x16_f16 v[98:113], v[196:199], v[130:133], v[98:113]
	global_load_lds_dwordx4 v154, s[6:7]
	s_add_i32 m0, s69, 0xa000
	v_mfma_f32_32x32x16_f16 v[98:113], v[208:211], v[134:137], v[98:113]
	global_load_lds_dwordx4 v250, s[6:7]
	s_add_i32 m0, s69, 0xc000
	v_mfma_f32_32x32x16_f16 v[98:113], v[220:223], v[138:141], v[98:113]
	global_load_lds_dwordx4 v251, s[6:7]
	s_add_i32 m0, s69, 0xe000
	v_mfma_f32_32x32x16_f16 v[98:113], v[236:239], v[142:145], v[98:113]
	global_load_lds_dwordx4 v252, s[6:7]
	s_add_i32 s4, s68, 0xffffff80
	s_cmp_le_i32 s4, s93
	v_add_u32_e32 v181, 0xffffff80, v179
	s_cbranch_scc1 .LBB1_14
	v_cmp_gt_i32_e64 s[62:63], 26, v181
	v_cmp_gt_i32_e64 s[64:65], 27, v181
	v_cmp_gt_i32_e64 s[60:61], 25, v181
	s_and_b64 s[62:63], s[64:65], s[62:63]
	v_cmp_gt_i32_e64 s[58:59], 24, v181
	s_and_b64 s[60:61], s[62:63], s[60:61]
	v_cmp_gt_i32_e64 s[56:57], 19, v181
	s_and_b64 s[58:59], s[60:61], s[58:59]
	v_cmp_gt_i32_e64 s[54:55], 18, v181
	s_and_b64 s[56:57], s[58:59], s[56:57]
	v_cmp_gt_i32_e64 s[52:53], 17, v181
	s_and_b64 s[54:55], s[56:57], s[54:55]
	v_cmp_gt_i32_e64 s[50:51], 16, v181
	s_and_b64 s[52:53], s[54:55], s[52:53]
	v_cmp_gt_i32_e64 s[48:49], 11, v181
	s_and_b64 s[50:51], s[52:53], s[50:51]
	v_cmp_gt_i32_e64 s[46:47], 10, v181
	s_and_b64 s[48:49], s[50:51], s[48:49]
	v_cmp_gt_i32_e64 s[44:45], 9, v181
	s_and_b64 s[46:47], s[48:49], s[46:47]
	v_cmp_gt_i32_e64 s[42:43], 8, v181
	s_and_b64 s[44:45], s[46:47], s[44:45]
	v_cmp_gt_i32_e64 s[40:41], 3, v181
	s_and_b64 s[42:43], s[44:45], s[42:43]
	v_cmp_gt_i32_e64 s[38:39], 2, v181
	s_and_b64 s[40:41], s[42:43], s[40:41]
	v_cmp_gt_i32_e64 s[36:37], 1, v181
	s_and_b64 s[38:39], s[40:41], s[38:39]
	v_cmp_gt_i32_e64 s[34:35], 0, v181
	s_and_b64 s[36:37], s[38:39], s[36:37]
	s_and_b64 s[34:35], s[36:37], s[34:35]
	v_cmp_gt_i32_e64 s[30:31], 58, v181
	v_cndmask_b32_e64 v82, v82, v164, s[34:35]
	v_cmp_gt_i32_e64 s[34:35], 59, v181
	v_cmp_gt_i32_e64 s[28:29], 57, v181
	s_and_b64 s[30:31], s[34:35], s[30:31]
	v_cmp_gt_i32_e64 s[26:27], 56, v181
	s_and_b64 s[28:29], s[30:31], s[28:29]
	v_cmp_gt_i32_e64 s[24:25], 51, v181
	s_and_b64 s[26:27], s[28:29], s[26:27]
	v_cmp_gt_i32_e64 s[22:23], 50, v181
	s_and_b64 s[24:25], s[26:27], s[24:25]
	v_cmp_gt_i32_e64 s[20:21], 49, v181
	s_and_b64 s[22:23], s[24:25], s[22:23]
	v_cmp_gt_i32_e64 s[18:19], 48, v181
	s_and_b64 s[20:21], s[22:23], s[20:21]
	v_cmp_gt_i32_e64 s[16:17], 43, v181
	s_and_b64 s[18:19], s[20:21], s[18:19]
	v_cmp_gt_i32_e64 s[14:15], 42, v181
	s_and_b64 s[16:17], s[18:19], s[16:17]
	v_cmp_gt_i32_e64 s[12:13], 41, v181
	s_and_b64 s[14:15], s[16:17], s[14:15]
	v_cmp_gt_i32_e64 s[10:11], 40, v181
	s_and_b64 s[12:13], s[14:15], s[12:13]
	v_cmp_gt_i32_e64 s[8:9], 35, v181
	s_and_b64 s[10:11], s[12:13], s[10:11]
	v_cmp_gt_i32_e64 s[6:7], 34, v181
	s_and_b64 s[8:9], s[10:11], s[8:9]
	v_cmp_gt_i32_e64 s[4:5], 33, v181
	s_and_b64 s[6:7], s[8:9], s[6:7]
	v_cmp_gt_i32_e32 vcc, 32, v181
	s_and_b64 s[4:5], s[6:7], s[4:5]
	s_and_b64 vcc, s[4:5], vcc
	v_cndmask_b32_e64 v97, v97, v164, s[64:65]
	v_cndmask_b32_e64 v96, v96, v164, s[62:63]
	v_cndmask_b32_e64 v95, v95, v164, s[60:61]
	v_cndmask_b32_e64 v94, v94, v164, s[58:59]
	v_cndmask_b32_e64 v93, v93, v164, s[56:57]
	v_cndmask_b32_e64 v92, v92, v164, s[54:55]
	v_cndmask_b32_e64 v91, v91, v164, s[52:53]
	v_cndmask_b32_e64 v90, v90, v164, s[50:51]
	v_cndmask_b32_e64 v89, v89, v164, s[48:49]
	v_cndmask_b32_e64 v88, v88, v164, s[46:47]
	v_cndmask_b32_e64 v87, v87, v164, s[44:45]
	v_cndmask_b32_e64 v86, v86, v164, s[42:43]
	v_cndmask_b32_e64 v85, v85, v164, s[40:41]
	v_cndmask_b32_e64 v84, v84, v164, s[38:39]
	v_cndmask_b32_e64 v83, v83, v164, s[36:37]
	v_cndmask_b32_e64 v113, v113, v164, s[34:35]
	v_cndmask_b32_e64 v112, v112, v164, s[30:31]
	v_cndmask_b32_e64 v111, v111, v164, s[28:29]
	v_cndmask_b32_e64 v110, v110, v164, s[26:27]
	v_cndmask_b32_e64 v109, v109, v164, s[24:25]
	v_cndmask_b32_e64 v108, v108, v164, s[22:23]
	v_cndmask_b32_e64 v107, v107, v164, s[20:21]
	v_cndmask_b32_e64 v106, v106, v164, s[18:19]
	v_cndmask_b32_e64 v105, v105, v164, s[16:17]
	v_cndmask_b32_e64 v104, v104, v164, s[14:15]
	v_cndmask_b32_e64 v103, v103, v164, s[12:13]
	v_cndmask_b32_e64 v102, v102, v164, s[10:11]
	v_cndmask_b32_e64 v101, v101, v164, s[8:9]
	v_cndmask_b32_e64 v100, v100, v164, s[6:7]
	v_cndmask_b32_e64 v99, v99, v164, s[4:5]
	v_cndmask_b32_e32 v98, v98, v164, vcc
.LBB1_14:
	ds_read_b64_tr_b16 v[182:183], v169 offset:0
	ds_read_b64_tr_b16 v[184:185], v169 offset:0x800
	ds_read_b64_tr_b16 v[186:187], v169 offset:0x1000
	ds_read_b64_tr_b16 v[188:189], v169 offset:0x1800
	ds_read_b64_tr_b16 v[190:191], v169 offset:0x2000
	ds_read_b64_tr_b16 v[192:193], v169 offset:0x2800
	ds_read_b64_tr_b16 v[194:195], v169 offset:0x3000
	ds_read_b64_tr_b16 v[196:197], v169 offset:0x3800
	v_fmac_f32 v83, 0x3f800000, v1
	v_fmac_f32 v84, 0x40000000, v1
	v_fmac_f32 v85, 0x40400000, v1
	v_fmac_f32 v86, 0x41000000, v1
	v_fmac_f32 v87, 0x41100000, v1
	s_nop 0
	s_waitcnt lgkmcnt(0)
	v_fmac_f32 v88, 0x41200000, v1
	v_fmac_f32 v89, 0x41300000, v1
	v_fmac_f32 v90, 0x41800000, v1
	v_fmac_f32 v91, 0x41880000, v1
	v_fmac_f32 v92, 0x41900000, v1
	s_nop 0
	v_mfma_f32_32x32x16_f16 v[50:65], v[4:7], v[182:185], v[50:65]
	ds_read_b64_tr_b16 v[182:183], v169 offset:0x200
	ds_read_b64_tr_b16 v[184:185], v169 offset:0xa00
	v_fmac_f32 v93, 0x41980000, v1
	v_fmac_f32 v94, 0x41c00000, v1
	v_fmac_f32 v95, 0x41c80000, v1
	v_fmac_f32 v96, 0x41d00000, v1
	v_fmac_f32 v97, 0x41d80000, v1
	v_mfma_f32_32x32x16_f16 v[50:65], v[8:11], v[186:189], v[50:65]
	ds_read_b64_tr_b16 v[186:187], v169 offset:0x1200
	ds_read_b64_tr_b16 v[188:189], v169 offset:0x1a00
	v_fmac_f32 v98, 0x42000000, v1
	v_fmac_f32 v99, 0x42040000, v1
	v_fmac_f32 v100, 0x42080000, v1
	v_fmac_f32 v101, 0x420c0000, v1
	v_fmac_f32 v102, 0x42200000, v1
	v_mfma_f32_32x32x16_f16 v[50:65], v[12:15], v[190:193], v[50:65]
	ds_read_b64_tr_b16 v[190:191], v169 offset:0x2200
	ds_read_b64_tr_b16 v[192:193], v169 offset:0x2a00
	v_fmac_f32 v103, 0x42240000, v1
	v_fmac_f32 v104, 0x42280000, v1
	v_fmac_f32 v105, 0x422c0000, v1
	v_fmac_f32 v106, 0x42400000, v1
	v_fmac_f32 v107, 0x42440000, v1
	v_mfma_f32_32x32x16_f16 v[50:65], v[146:149], v[194:197], v[50:65]
	ds_read_b64_tr_b16 v[194:195], v169 offset:0x3200
	ds_read_b64_tr_b16 v[196:197], v169 offset:0x3a00
	v_fmac_f32 v108, 0x42480000, v1
	v_fmac_f32 v109, 0x424c0000, v1
	v_fmac_f32 v110, 0x42600000, v1
	v_fmac_f32 v111, 0x42640000, v1
	v_fmac_f32 v112, 0x42680000, v1
	s_nop 0
	s_waitcnt lgkmcnt(0)
	ds_read_b64_tr_b16 v[198:199], v169 offset:0x400
	ds_read_b64_tr_b16 v[200:201], v169 offset:0xc00
	ds_read_b64_tr_b16 v[202:203], v169 offset:0x1400
	ds_read_b64_tr_b16 v[204:205], v169 offset:0x1c00
	ds_read_b64_tr_b16 v[206:207], v169 offset:0x2400
	s_nop 0
	v_mfma_f32_32x32x16_f16 v[18:33], v[4:7], v[182:185], v[18:33]
	ds_read_b64_tr_b16 v[208:209], v169 offset:0x2c00
	ds_read_b64_tr_b16 v[184:185], v169 offset:0x3400
	v_cvt_f32_i32_e32 v183, v181
	v_max_f32_e32 v181, v83, v83
	v_max_f32_e32 v182, v82, v82
	v_max_f32_e32 v181, v182, v181
	v_max3_f32 v181, v181, v84, v85
	v_mfma_f32_32x32x16_f16 v[18:33], v[8:11], v[186:189], v[18:33]
	ds_read_b64_tr_b16 v[186:187], v169 offset:0x3c00
	v_max3_f32 v181, v181, v86, v87
	s_waitcnt lgkmcnt(0)
	ds_read_b64_tr_b16 v[210:211], v169 offset:0x600
	ds_read_b64_tr_b16 v[212:213], v169 offset:0xe00
	ds_read_b64_tr_b16 v[214:215], v169 offset:0x1600
	ds_read_b64_tr_b16 v[216:217], v169 offset:0x1e00
	ds_read_b64_tr_b16 v[188:189], v169 offset:0x2600
	v_mfma_f32_32x32x16_f16 v[18:33], v[12:15], v[190:193], v[18:33]
	ds_read_b64_tr_b16 v[190:191], v169 offset:0x2e00
	ds_read_b64_tr_b16 v[218:219], v169 offset:0x3600
	ds_read_b64_tr_b16 v[220:221], v169 offset:0x3e00
	v_max3_f32 v181, v181, v88, v89
	s_waitcnt lgkmcnt(0)
	v_fmac_f32 v113, 0x426c0000, v1
	v_mfma_f32_32x32x16_f16 v[66:81], v[4:7], v[198:201], v[66:81]
	v_mfma_f32_32x32x16_f16 v[34:49], v[4:7], v[210:213], v[34:49]
	v_max3_f32 v4, v181, v90, v91
	v_max3_f32 v4, v4, v92, v93
	v_max3_f32 v4, v4, v94, v95
	v_max3_f32 v4, v4, v96, v97
	v_max3_f32 v4, v4, v98, v99
	v_max3_f32 v4, v4, v100, v101
	v_max3_f32 v4, v4, v102, v103
	v_mfma_f32_32x32x16_f16 v[66:81], v[8:11], v[202:205], v[66:81]
	v_max3_f32 v4, v4, v104, v105
	v_max3_f32 v4, v4, v106, v107
	v_max3_f32 v4, v4, v108, v109
	v_max3_f32 v4, v4, v110, v111
	v_max3_f32 v4, v4, v112, v113
	v_fma_f32 v4, -v1, v183, v4
	v_mov_b32_e32 v5, v4
	v_mfma_f32_32x32x16_f16 v[34:49], v[8:11], v[214:217], v[34:49]
	s_nop 0
	v_permlane32_swap_b32_e32 v4, v5
	v_max3_f32 v182, v178, v4, v5
	v_sub_f32_e32 v4, v178, v182
	v_mul_f32_e32 v4, 0x3e0293ee, v4
	v_exp_f32_e32 v181, v4
	v_mfma_f32_32x32x16_f16 v[66:81], v[12:15], v[206:209], v[66:81]
	v_cmp_gt_f32_e32 vcc, 0xc1000000, v4
	v_mfma_f32_32x32x16_f16 v[34:49], v[12:15], v[188:191], v[34:49]
	v_mfma_f32_32x32x16_f16 v[18:33], v[146:149], v[194:197], v[18:33]
	v_mfma_f32_32x32x16_f16 v[66:81], v[146:149], v[184:187], v[66:81]
	v_mfma_f32_32x32x16_f16 v[34:49], v[146:149], v[218:221], v[34:49]
	s_cbranch_vccz .Llazy1
	s_and_saveexec_b64 s[4:5], s[2:3]
	ds_write_b32 v176, v181 offset:128
	s_or_b64 exec, exec, s[4:5]
	ds_read_b128 v[198:201], v177 offset:224
	ds_read_b128 v[202:205], v177 offset:192
	ds_read_b128 v[206:209], v177 offset:160
	ds_read_b128 v[210:213], v177 offset:128
	s_branch .LBB1_18
.Llazy1:
	v_mov_b32_e32 v182, v178
	v_mov_b32_e32 v181, 1.0

.LBB1_22:
	ds_read_b64_tr_b16 v[184:185], v169 offset:0x8000
	ds_read_b64_tr_b16 v[186:187], v169 offset:0x8800
	ds_read_b64_tr_b16 v[188:189], v169 offset:0x9000
	ds_read_b64_tr_b16 v[190:191], v169 offset:0x9800
	ds_read_b64_tr_b16 v[194:195], v169 offset:0xa000
	ds_read_b64_tr_b16 v[196:197], v169 offset:0xa800
	ds_read_b64_tr_b16 v[198:199], v169 offset:0xb000
	ds_read_b64_tr_b16 v[200:201], v169 offset:0xb800
	v_fmac_f32 v99, 0x3f800000, v1
	v_max_f32_e32 v156, v98, v98
	s_waitcnt lgkmcnt(0)
	v_max_f32_e32 v17, v99, v99
	v_mfma_f32_32x32x16_f16 v[50:65], v[4:7], v[184:187], v[50:65]
	ds_read_b64_tr_b16 v[184:185], v169 offset:0x8200
	ds_read_b64_tr_b16 v[186:187], v169 offset:0x8a00
	v_max_f32_e32 v17, v156, v17
	v_fmac_f32 v100, 0x40000000, v1
	v_fmac_f32 v101, 0x40400000, v1
	v_fmac_f32 v102, 0x41000000, v1
	v_fmac_f32 v103, 0x41100000, v1
	v_mfma_f32_32x32x16_f16 v[50:65], v[8:11], v[188:191], v[50:65]
	ds_read_b64_tr_b16 v[188:189], v169 offset:0x9200
	ds_read_b64_tr_b16 v[190:191], v169 offset:0x9a00
	v_max3_f32 v17, v17, v100, v101
	v_max3_f32 v17, v17, v102, v103
	v_fmac_f32 v104, 0x41200000, v1
	v_fmac_f32 v105, 0x41300000, v1
	v_fmac_f32 v106, 0x41800000, v1
	v_mfma_f32_32x32x16_f16 v[50:65], v[12:15], v[194:197], v[50:65]
	ds_read_b64_tr_b16 v[194:195], v169 offset:0xa200
	ds_read_b64_tr_b16 v[196:197], v169 offset:0xaa00
	v_max3_f32 v17, v17, v104, v105
	v_fmac_f32 v107, 0x41880000, v1
	v_fmac_f32 v108, 0x41900000, v1
	v_fmac_f32 v109, 0x41980000, v1
	v_fmac_f32 v110, 0x41c00000, v1
	v_mfma_f32_32x32x16_f16 v[50:65], v[146:149], v[198:201], v[50:65]
	ds_read_b64_tr_b16 v[198:199], v169 offset:0xb200
	ds_read_b64_tr_b16 v[200:201], v169 offset:0xba00
	v_fmac_f32 v111, 0x41c80000, v1
	v_fmac_f32 v112, 0x41d00000, v1
	v_fmac_f32 v113, 0x41d80000, v1
	v_fmac_f32 v82, 0x42000000, v1
	v_fmac_f32 v83, 0x42040000, v1
	s_nop 0
	s_waitcnt lgkmcnt(0)
	v_fmac_f32 v84, 0x42080000, v1
	v_fmac_f32 v85, 0x420c0000, v1
	v_fmac_f32 v86, 0x42200000, v1
	v_fmac_f32 v87, 0x42240000, v1
	v_fmac_f32 v88, 0x42280000, v1
	s_nop 0
	v_mfma_f32_32x32x16_f16 v[18:33], v[4:7], v[184:187], v[18:33]
	ds_read_b64_tr_b16 v[184:185], v169 offset:0x8400
	ds_read_b64_tr_b16 v[186:187], v169 offset:0x8c00
	ds_read_b64_tr_b16 v[202:203], v169 offset:0x9400
	ds_read_b64_tr_b16 v[204:205], v169 offset:0x9c00
	ds_read_b64_tr_b16 v[206:207], v169 offset:0xa400
	ds_read_b64_tr_b16 v[208:209], v169 offset:0xac00
	ds_read_b64_tr_b16 v[210:211], v169 offset:0xb400
	v_mfma_f32_32x32x16_f16 v[18:33], v[8:11], v[188:191], v[18:33]
	ds_read_b64_tr_b16 v[212:213], v169 offset:0xbc00
	v_fmac_f32 v89, 0x422c0000, v1
	v_cvt_f32_i32_e32 v16, v179
	s_waitcnt lgkmcnt(0)
	ds_read_b64_tr_b16 v[188:189], v169 offset:0x8600
	ds_read_b64_tr_b16 v[190:191], v169 offset:0x8e00
	ds_read_b64_tr_b16 v[214:215], v169 offset:0x9600
	ds_read_b64_tr_b16 v[216:217], v169 offset:0x9e00
	ds_read_b64_tr_b16 v[218:219], v169 offset:0xa600
	ds_read_b64_tr_b16 v[220:221], v169 offset:0xae00
	v_mfma_f32_32x32x16_f16 v[18:33], v[12:15], v[194:197], v[18:33]
	ds_read_b64_tr_b16 v[194:195], v169 offset:0xb600
	ds_read_b64_tr_b16 v[196:197], v169 offset:0xbe00
	v_fmac_f32 v90, 0x42400000, v1
	v_fmac_f32 v91, 0x42440000, v1
	v_fmac_f32 v92, 0x42480000, v1
	v_fmac_f32 v93, 0x424c0000, v1
	v_fmac_f32 v94, 0x42600000, v1
	s_nop 0
	s_waitcnt lgkmcnt(0)
	v_mfma_f32_32x32x16_f16 v[66:81], v[4:7], v[184:187], v[66:81]
	v_fmac_f32 v95, 0x42640000, v1
	v_fmac_f32 v96, 0x42680000, v1
	v_fmac_f32 v97, 0x426c0000, v1
	v_mfma_f32_32x32x16_f16 v[34:49], v[4:7], v[188:191], v[34:49]
	v_max3_f32 v4, v17, v106, v107
	v_max3_f32 v4, v4, v108, v109
	v_max3_f32 v4, v4, v110, v111
	v_max3_f32 v4, v4, v112, v113
	v_max3_f32 v4, v4, v82, v83
	v_max3_f32 v4, v4, v84, v85
	v_max3_f32 v4, v4, v86, v87
	v_mfma_f32_32x32x16_f16 v[66:81], v[8:11], v[202:205], v[66:81]
	v_max3_f32 v4, v4, v88, v89
	v_max3_f32 v4, v4, v90, v91
	v_max3_f32 v4, v4, v92, v93
	v_max3_f32 v4, v4, v94, v95
	v_max3_f32 v4, v4, v96, v97
	v_fma_f32 v4, -v1, v16, v4
	v_mov_b32_e32 v5, v4
	v_mfma_f32_32x32x16_f16 v[34:49], v[8:11], v[214:217], v[34:49]
	s_nop 0
	v_permlane32_swap_b32_e32 v4, v5
	v_max3_f32 v178, v182, v4, v5
	v_sub_f32_e32 v4, v182, v178
	v_mul_f32_e32 v4, 0x3e0293ee, v4
	v_exp_f32_e32 v5, v4
	v_mfma_f32_32x32x16_f16 v[66:81], v[12:15], v[206:209], v[66:81]
	v_cmp_gt_f32_e32 vcc, 0xc1000000, v4
	v_mfma_f32_32x32x16_f16 v[34:49], v[12:15], v[218:221], v[34:49]
	v_mfma_f32_32x32x16_f16 v[18:33], v[146:149], v[198:201], v[18:33]
	v_mfma_f32_32x32x16_f16 v[66:81], v[146:149], v[210:213], v[66:81]
	v_mfma_f32_32x32x16_f16 v[34:49], v[146:149], v[194:197], v[34:49]
	s_cbranch_vccz .Llazy2
	s_and_saveexec_b64 s[4:5], s[2:3]
	s_cbranch_execz .LBB1_10
	ds_write_b32 v176, v5 offset:128
	s_branch .LBB1_10

.LBB1_28:
	ds_read_b128 v[4:7], v172 offset:32768
	ds_read_b128 v[8:11], v249 offset:32768
	ds_read_b128 v[192:195], v172 offset:40960
	ds_read_b128 v[196:199], v249 offset:40960
	ds_read_b128 v[12:15], v173 offset:32768
	ds_read_b128 v[200:203], v253 offset:32768
	ds_read_b128 v[204:207], v173 offset:40960
	ds_read_b128 v[208:211], v253 offset:40960
	s_waitcnt lgkmcnt(7)
	v_mfma_f32_32x32x16_f16 v[82:97], v[4:7], v[114:117], 0
	ds_read_b128 v[4:7], v174 offset:32768
	ds_read_b128 v[212:215], v254 offset:32768
	ds_read_b128 v[216:219], v174 offset:40960
	ds_read_b128 v[220:223], v254 offset:40960
	ds_read_b128 v[224:227], v175 offset:32768
	ds_read_b128 v[228:231], v255 offset:32768
	ds_read_b128 v[232:235], v175 offset:40960
	ds_read_b128 v[172:175], v255 offset:40960
	v_exp_f32_e32 v3, v98
	v_exp_f32_e32 v98, v103
	v_exp_f32_e32 v103, v108
	v_exp_f32_e32 v108, v113
	s_waitcnt lgkmcnt(11)
	v_mfma_f32_32x32x16_f16 v[82:97], v[12:15], v[118:121], v[82:97]
	v_exp_f32_e32 v12, v99
	v_exp_f32_e32 v13, v100
	v_exp_f32_e32 v14, v101
	v_exp_f32_e32 v15, v102
	v_exp_f32_e32 v99, v104
	v_exp_f32_e32 v100, v105
	v_exp_f32_e32 v101, v106
	s_waitcnt lgkmcnt(7)
	v_mfma_f32_32x32x16_f16 v[82:97], v[4:7], v[122:125], v[82:97]
	v_add_f32_e32 v4, 0, v190
	v_add_f32_e32 v4, v191, v4
	v_add_f32_e32 v4, v188, v4
	v_add_f32_e32 v4, v189, v4
	v_add_f32_e32 v4, v186, v4
	v_add_f32_e32 v4, v187, v4
	v_add_f32_e32 v4, v184, v4
	s_waitcnt lgkmcnt(3)
	v_mfma_f32_32x32x16_f16 v[82:97], v[224:227], v[126:129], v[82:97]
	v_add_f32_e32 v4, v185, v4
	v_add_f32_e32 v4, v182, v4
	v_add_f32_e32 v4, v183, v4
	v_add_f32_e32 v4, v156, v4
	v_add_f32_e32 v4, v157, v4
	v_add_f32_e32 v4, v148, v4
	v_add_f32_e32 v4, v149, v4
	v_mfma_f32_32x32x16_f16 v[82:97], v[8:11], v[130:133], v[82:97]
	v_add_f32_e32 v4, v146, v4
	v_add_f32_e32 v4, v147, v4
	v_add_f32_e32 v4, v3, v4
	v_add_f32_e32 v4, v12, v4
	v_add_f32_e32 v4, v13, v4
	v_add_f32_e32 v4, v14, v4
	v_add_f32_e32 v4, v15, v4
	v_mfma_f32_32x32x16_f16 v[82:97], v[200:203], v[134:137], v[82:97]
	v_exp_f32_e32 v102, v107
	v_add_f32_e32 v4, v98, v4
	v_add_f32_e32 v4, v99, v4
	v_exp_f32_e32 v104, v109
	v_add_f32_e32 v4, v100, v4
	v_exp_f32_e32 v105, v110
	v_add_f32_e32 v4, v101, v4
	v_mfma_f32_32x32x16_f16 v[82:97], v[212:215], v[138:141], v[82:97]
	v_exp_f32_e32 v106, v111
	v_add_f32_e32 v4, v102, v4
	v_exp_f32_e32 v107, v112
	v_add_f32_e32 v4, v103, v4
	v_add_f32_e32 v4, v104, v4
	v_add_f32_e32 v4, v105, v4
	v_add_f32_e32 v4, v106, v4
	s_waitcnt lgkmcnt(2)
	v_mfma_f32_32x32x16_f16 v[82:97], v[228:231], v[142:145], v[82:97]
	v_add_f32_e32 v4, v107, v4
	v_add_f32_e32 v16, v108, v4
	v_mov_b32_e32 v17, v16
	v_cvt_pk_f16_f32 v4, v190, v191
	v_cvt_pk_f16_f32 v5, v188, v189
	v_cvt_pk_f16_f32 v6, v186, v187
	v_cvt_pk_f16_f32 v7, v184, v185
	v_cvt_pk_f16_f32 v8, v182, v183
	v_cvt_pk_f16_f32 v9, v156, v157
	v_cvt_pk_f16_f32 v10, v148, v149
	v_cvt_pk_f16_f32 v11, v146, v147
	v_cvt_pk_f16_f32 v12, v3, v12
	v_cvt_pk_f16_f32 v13, v13, v14
	v_cvt_pk_f16_f32 v14, v15, v98
	v_cvt_pk_f16_f32 v15, v99, v100
	v_cvt_pk_f16_f32 v146, v101, v102
	v_cvt_pk_f16_f32 v147, v103, v104
	v_cvt_pk_f16_f32 v148, v105, v106
	v_cvt_pk_f16_f32 v149, v107, v108
	s_nop 1
	v_permlane32_swap_b32_e32 v16, v17
	v_permlane32_swap_b32_e32 v4, v6
	v_permlane32_swap_b32_e32 v5, v7
	v_permlane32_swap_b32_e32 v8, v10
	v_permlane32_swap_b32_e32 v9, v11
	v_permlane32_swap_b32_e32 v12, v14
	v_permlane32_swap_b32_e32 v13, v15
	v_permlane32_swap_b32_e32 v146, v148
	v_permlane32_swap_b32_e32 v147, v149
	s_lshl_b64 s[2:3], s[72:73], 15
	s_add_u32 s2, s76, s2
	s_addc_u32 s3, s77, s3
	v_lshl_add_u64 v[154:155], v[152:153], 1, s[2:3]
	s_lshl_b32 s2, s33, 10
	s_add_i32 s2, s2, 0
	s_add_i32 m0, s2, 0x8000
	s_mov_b64 s[4:5], 0x2000
	global_load_lds_dwordx4 v[154:155], off
	v_lshl_add_u64 v[156:157], v[154:155], 0, s[4:5]
	s_add_i32 m0, s2, 0xa000
	s_mov_b64 s[4:5], 0x4000
	global_load_lds_dwordx4 v[156:157], off
	v_lshl_add_u64 v[156:157], v[154:155], 0, s[4:5]
	s_add_i32 m0, s2, 0xc000
	s_mov_b64 s[4:5], 0x6000
	global_load_lds_dwordx4 v[156:157], off
	v_lshl_add_u64 v[154:155], v[154:155], 0, s[4:5]
	s_add_i32 m0, s2, 0xe000
	v_mfma_f32_32x32x16_f16 v[98:113], v[192:195], v[114:117], 0
	global_load_lds_dwordx4 v[154:155], off
	v_mfma_f32_32x32x16_f16 v[98:113], v[204:207], v[118:121], v[98:113]
	v_mfma_f32_32x32x16_f16 v[98:113], v[216:219], v[122:125], v[98:113]
	s_waitcnt lgkmcnt(0)
	v_mfma_f32_32x32x16_f16 v[98:113], v[232:235], v[126:129], v[98:113]
	v_mfma_f32_32x32x16_f16 v[98:113], v[196:199], v[130:133], v[98:113]
	v_mfma_f32_32x32x16_f16 v[98:113], v[208:211], v[134:137], v[98:113]
	v_mfma_f32_32x32x16_f16 v[98:113], v[220:223], v[138:141], v[98:113]
	v_mfma_f32_32x32x16_f16 v[98:113], v[172:175], v[142:145], v[98:113]
	s_lshl_b32 s2, s72, 7
	s_sub_i32 s2, s82, s2
	s_or_b32 s3, s2, 63
	s_cmp_le_i32 s3, s93
	v_subrev_u32_e32 v3, s2, v171
	s_cbranch_scc1 .LBB1_30
	v_cmp_gt_i32_e64 s[60:61], 26, v3
	v_cmp_gt_i32_e64 s[62:63], 27, v3
	v_cmp_gt_i32_e64 s[58:59], 25, v3
	s_and_b64 s[60:61], s[62:63], s[60:61]
	v_cmp_gt_i32_e64 s[56:57], 24, v3
	s_and_b64 s[58:59], s[60:61], s[58:59]
	v_cmp_gt_i32_e64 s[54:55], 19, v3
	s_and_b64 s[56:57], s[58:59], s[56:57]
	v_cmp_gt_i32_e64 s[52:53], 18, v3
	s_and_b64 s[54:55], s[56:57], s[54:55]
	v_cmp_gt_i32_e64 s[50:51], 17, v3
	s_and_b64 s[52:53], s[54:55], s[52:53]
	v_cmp_gt_i32_e64 s[48:49], 16, v3
	s_and_b64 s[50:51], s[52:53], s[50:51]
	v_cmp_gt_i32_e64 s[46:47], 11, v3
	s_and_b64 s[48:49], s[50:51], s[48:49]
	v_cmp_gt_i32_e64 s[44:45], 10, v3
	s_and_b64 s[46:47], s[48:49], s[46:47]
	v_cmp_gt_i32_e64 s[42:43], 9, v3
	s_and_b64 s[44:45], s[46:47], s[44:45]
	v_cmp_gt_i32_e64 s[40:41], 8, v3
	s_and_b64 s[42:43], s[44:45], s[42:43]
	v_cmp_gt_i32_e64 s[38:39], 3, v3
	s_and_b64 s[40:41], s[42:43], s[40:41]
	v_cmp_gt_i32_e64 s[36:37], 2, v3
	s_and_b64 s[38:39], s[40:41], s[38:39]
	v_cmp_gt_i32_e64 s[34:35], 1, v3
	s_and_b64 s[36:37], s[38:39], s[36:37]
	v_cmp_gt_i32_e64 s[30:31], 0, v3
	s_and_b64 s[34:35], s[36:37], s[34:35]
	s_and_b64 s[30:31], s[34:35], s[30:31]
	v_cmp_gt_i32_e64 s[28:29], 58, v3
	v_cndmask_b32_e64 v82, v82, v164, s[30:31]
	v_cmp_gt_i32_e64 s[30:31], 59, v3
	v_cmp_gt_i32_e64 s[26:27], 57, v3
	s_and_b64 s[28:29], s[30:31], s[28:29]
	v_cmp_gt_i32_e64 s[24:25], 56, v3
	s_and_b64 s[26:27], s[28:29], s[26:27]
	v_cmp_gt_i32_e64 s[22:23], 51, v3
	s_and_b64 s[24:25], s[26:27], s[24:25]
	v_cmp_gt_i32_e64 s[20:21], 50, v3
	s_and_b64 s[22:23], s[24:25], s[22:23]
	v_cmp_gt_i32_e64 s[18:19], 49, v3
	s_and_b64 s[20:21], s[22:23], s[20:21]
	v_cmp_gt_i32_e64 s[16:17], 48, v3
	s_and_b64 s[18:19], s[20:21], s[18:19]
	v_cmp_gt_i32_e64 s[14:15], 43, v3
	s_and_b64 s[16:17], s[18:19], s[16:17]
	v_cmp_gt_i32_e64 s[12:13], 42, v3
	s_and_b64 s[14:15], s[16:17], s[14:15]
	v_cmp_gt_i32_e64 s[10:11], 41, v3
	s_and_b64 s[12:13], s[14:15], s[12:13]
	v_cmp_gt_i32_e64 s[8:9], 40, v3
	s_and_b64 s[10:11], s[12:13], s[10:11]
	v_cmp_gt_i32_e64 s[6:7], 35, v3
	s_and_b64 s[8:9], s[10:11], s[8:9]
	v_cmp_gt_i32_e64 s[4:5], 34, v3
	s_and_b64 s[6:7], s[8:9], s[6:7]
	v_cmp_gt_i32_e64 s[2:3], 33, v3
	s_and_b64 s[4:5], s[6:7], s[4:5]
	v_cmp_gt_i32_e32 vcc, 32, v3
	s_and_b64 s[2:3], s[4:5], s[2:3]
	s_and_b64 vcc, s[2:3], vcc
	v_cndmask_b32_e64 v97, v97, v164, s[62:63]
	v_cndmask_b32_e64 v96, v96, v164, s[60:61]
	v_cndmask_b32_e64 v95, v95, v164, s[58:59]
	v_cndmask_b32_e64 v94, v94, v164, s[56:57]
	v_cndmask_b32_e64 v93, v93, v164, s[54:55]
	v_cndmask_b32_e64 v92, v92, v164, s[52:53]
	v_cndmask_b32_e64 v91, v91, v164, s[50:51]
	v_cndmask_b32_e64 v90, v90, v164, s[48:49]
	v_cndmask_b32_e64 v89, v89, v164, s[46:47]
	v_cndmask_b32_e64 v88, v88, v164, s[44:45]
	v_cndmask_b32_e64 v87, v87, v164, s[42:43]
	v_cndmask_b32_e64 v86, v86, v164, s[40:41]
	v_cndmask_b32_e64 v85, v85, v164, s[38:39]
	v_cndmask_b32_e64 v84, v84, v164, s[36:37]
	v_cndmask_b32_e64 v83, v83, v164, s[34:35]
	v_cndmask_b32_e64 v113, v113, v164, s[30:31]
	v_cndmask_b32_e64 v112, v112, v164, s[28:29]
	v_cndmask_b32_e64 v111, v111, v164, s[26:27]
	v_cndmask_b32_e64 v110, v110, v164, s[24:25]
	v_cndmask_b32_e64 v109, v109, v164, s[22:23]
	v_cndmask_b32_e64 v108, v108, v164, s[20:21]
	v_cndmask_b32_e64 v107, v107, v164, s[18:19]
	v_cndmask_b32_e64 v106, v106, v164, s[16:17]
	v_cndmask_b32_e64 v105, v105, v164, s[14:15]
	v_cndmask_b32_e64 v104, v104, v164, s[12:13]
	v_cndmask_b32_e64 v103, v103, v164, s[10:11]
	v_cndmask_b32_e64 v102, v102, v164, s[8:9]
	v_cndmask_b32_e64 v101, v101, v164, s[6:7]
	v_cndmask_b32_e64 v100, v100, v164, s[4:5]
	v_cndmask_b32_e64 v99, v99, v164, s[2:3]
	v_cndmask_b32_e32 v98, v98, v164, vcc

.LBB1_35:
	v_readlane_b32 s4, v248, 21
	s_nop 3
	s_lshl_b32 s4, s4, 1
	s_sub_i32 s4, 15, s4
	s_lshl_b32 s4, s4, 15
	s_add_u32 s74, s74, s4
	s_addc_u32 s75, s75, 0
	s_add_u32 s76, s76, s4
	s_addc_u32 s77, s77, 0
	v_writelane_b32 v248, s74, 22
	v_writelane_b32 v248, s75, 23
	s_add_u32 s6, s74, 0x8000
	s_addc_u32 s7, s75, 0
	v_writelane_b32 v248, s6, 6
	v_writelane_b32 v248, s7, 7
	s_add_u32 s6, s74, 0xa000
	s_addc_u32 s7, s75, 0
	v_writelane_b32 v248, s6, 8
	v_writelane_b32 v248, s7, 9
	s_add_u32 s6, s74, 0xc000
	s_addc_u32 s7, s75, 0
	v_writelane_b32 v248, s6, 10
	v_writelane_b32 v248, s7, 11
	s_add_u32 s6, s74, 0xe000
	s_addc_u32 s7, s75, 0
	v_writelane_b32 v248, s6, 12
	v_writelane_b32 v248, s7, 13
	s_lshl_b32 s2, s33, 10
	s_add_i32 s2, s2, 0
	v_lshl_add_u64 v[6:7], v[152:153], 1, s[74:75]
	s_add_i32 m0, s2, 0x10000
	s_mov_b64 s[4:5], 0x2000
	global_load_lds_dwordx4 v[6:7], off
	v_lshl_add_u64 v[8:9], v[6:7], 0, s[4:5]
	s_add_i32 m0, s2, 0x12000
	s_mov_b64 s[4:5], 0x4000
	global_load_lds_dwordx4 v[8:9], off
	v_lshl_add_u64 v[8:9], v[6:7], 0, s[4:5]
	s_add_i32 m0, s2, 0x14000
	s_mov_b64 s[4:5], 0x6000
	global_load_lds_dwordx4 v[8:9], off
	v_lshl_add_u64 v[6:7], v[6:7], 0, s[4:5]
	s_add_i32 m0, s2, 0x16000
	v_readlane_b32 s4, v248, 17
	global_load_lds_dwordx4 v[6:7], off
	v_readlane_b32 s5, v248, 18
	s_andn2_b64 vcc, exec, s[4:5]
	s_cbranch_vccnz .LBB1_37
	v_readlane_b32 s4, v248, 6
	v_lshlrev_b64 v[6:7], 1, v[152:153]
	v_readlane_b32 s5, v248, 7
	s_add_i32 m0, s2, 0x18000
	s_nop 0
	v_lshl_add_u64 v[8:9], s[4:5], 0, v[6:7]
	v_readlane_b32 s4, v248, 8
	v_readlane_b32 s5, v248, 9
	global_load_lds_dwordx4 v[8:9], off
	s_nop 0
	v_lshl_add_u64 v[8:9], s[4:5], 0, v[6:7]
	v_readlane_b32 s4, v248, 10
	s_add_i32 m0, s2, 0x1a000
	v_readlane_b32 s5, v248, 11
	global_load_lds_dwordx4 v[8:9], off
	s_nop 0
	v_lshl_add_u64 v[8:9], s[4:5], 0, v[6:7]
	v_readlane_b32 s4, v248, 12
	s_add_i32 m0, s2, 0x1c000
	v_readlane_b32 s5, v248, 13
	global_load_lds_dwordx4 v[8:9], off
	s_nop 0
	v_lshl_add_u64 v[6:7], s[4:5], 0, v[6:7]
	s_add_i32 m0, s2, 0x1e000
	s_nop 0
	global_load_lds_dwordx4 v[6:7], off

	.amdhsa_kernel _Z11attn_kernelPKDF16_S0_S0_PDF16_PKfS1_
		.amdhsa_group_segment_fixed_size 0
		.amdhsa_private_segment_fixed_size 0
		.amdhsa_kernarg_size 48
		.amdhsa_user_sgpr_count 2
		.amdhsa_user_sgpr_dispatch_ptr 0
		.amdhsa_user_sgpr_queue_ptr 0
		.amdhsa_user_sgpr_kernarg_segment_ptr 1
		.amdhsa_user_sgpr_dispatch_id 0
		.amdhsa_user_sgpr_kernarg_preload_length 0
		.amdhsa_user_sgpr_kernarg_preload_offset 0
		.amdhsa_user_sgpr_private_segment_size 0
		.amdhsa_uses_dynamic_stack 0
		.amdhsa_enable_private_segment 0
		.amdhsa_system_sgpr_workgroup_id_x 1
		.amdhsa_system_sgpr_workgroup_id_y 0
		.amdhsa_system_sgpr_workgroup_id_z 0
		.amdhsa_system_sgpr_workgroup_info 0
		.amdhsa_system_vgpr_workitem_id 0
		.amdhsa_next_free_vgpr 256
		.amdhsa_next_free_sgpr 101
		.amdhsa_accum_offset 256
		.amdhsa_reserve_vcc 1
		.amdhsa_float_round_mode_32 0
		.amdhsa_float_round_mode_16_64 0
		.amdhsa_float_denorm_mode_32 3
		.amdhsa_float_denorm_mode_16_64 3
		.amdhsa_dx10_clamp 1
		.amdhsa_ieee_mode 1
		.amdhsa_fp16_overflow 0
		.amdhsa_tg_split 0
		.amdhsa_exception_fp_ieee_invalid_op 0
		.amdhsa_exception_fp_denorm_src 0
		.amdhsa_exception_fp_ieee_div_zero 0
		.amdhsa_exception_fp_ieee_overflow 0
		.amdhsa_exception_fp_ieee_underflow 0
		.amdhsa_exception_fp_ieee_inexact 0
		.amdhsa_exception_int_div_zero 0
	.end_amdhsa_kernel

.LBB2_15:
	s_waitcnt lgkmcnt(0)
	s_and_b32 s46, s3, 15
	s_lshl_b32 s46, s46, 1
	s_sub_i32 s46, 15, s46
	s_lshl_b32 s46, s46, 15
	s_ashr_i32 s47, s46, 31
	s_add_u32 s10, s10, s46
	s_addc_u32 s11, s11, s47
	s_add_u32 s12, s12, s46
	s_addc_u32 s13, s13, s47
	global_load_dwordx4 v[126:129], v98, s[20:21]
	global_load_dwordx4 v[122:125], v98, s[22:23]
	global_load_dwordx4 v[118:121], v101, s[20:21]
	global_load_dwordx4 v[110:113], v101, s[22:23]
	global_load_dwordx4 v[106:109], v100, s[20:21]
	global_load_dwordx4 v[114:117], v100, s[22:23]
	global_load_dwordx4 v[102:105], v99, s[20:21]
	s_nop 0
	global_load_dwordx4 v[98:101], v99, s[22:23]
	s_andn2_b64 vcc, exec, s[26:27]
	s_cbranch_vccnz .LBB2_17
	s_ashr_i32 s5, s4, 31
	s_lshl_b64 s[4:5], s[4:5], 2
	s_add_u32 s24, s14, s4
	s_addc_u32 s25, s15, s5

	.amdhsa_kernel _Z11k_gemm_a1b3IN3pg87EpiQKV3EEvNS0_4GemmET_
		.amdhsa_group_segment_fixed_size 0
		.amdhsa_private_segment_fixed_size 0
		.amdhsa_kernarg_size 96
		.amdhsa_user_sgpr_count 2
		.amdhsa_user_sgpr_dispatch_ptr 0
		.amdhsa_user_sgpr_queue_ptr 0
		.amdhsa_user_sgpr_kernarg_segment_ptr 1
		.amdhsa_user_sgpr_dispatch_id 0
		.amdhsa_user_sgpr_kernarg_preload_length 0
		.amdhsa_user_sgpr_kernarg_preload_offset 0
		.amdhsa_user_sgpr_private_segment_size 0
		.amdhsa_uses_dynamic_stack 0
		.amdhsa_enable_private_segment 0
		.amdhsa_system_sgpr_workgroup_id_x 1
		.amdhsa_system_sgpr_workgroup_id_y 0
		.amdhsa_system_sgpr_workgroup_id_z 0
		.amdhsa_system_sgpr_workgroup_info 0
		.amdhsa_system_vgpr_workitem_id 0
		.amdhsa_next_free_vgpr 168
		.amdhsa_next_free_sgpr 48
		.amdhsa_accum_offset 168
		.amdhsa_reserve_vcc 1
		.amdhsa_float_round_mode_32 0
		.amdhsa_float_round_mode_16_64 0
		.amdhsa_float_denorm_mode_32 3
		.amdhsa_float_denorm_mode_16_64 3
		.amdhsa_dx10_clamp 1
		.amdhsa_ieee_mode 1
		.amdhsa_fp16_overflow 0
		.amdhsa_tg_split 0
		.amdhsa_exception_fp_ieee_invalid_op 0
		.amdhsa_exception_fp_denorm_src 0
		.amdhsa_exception_fp_ieee_div_zero 0
		.amdhsa_exception_fp_ieee_overflow 0
		.amdhsa_exception_fp_ieee_underflow 0
		.amdhsa_exception_fp_ieee_inexact 0
		.amdhsa_exception_int_div_zero 0
	.end_amdhsa_kernel
